# att8_softmax_valu_into_kread_bubble_and_early_vreads
# baseline (speedup 1.0000x reference)
.LBB0_823:
	s_lshl_b32 s2, s42, 13
	s_add_i32 s2, s2, 0
	v_add_u32_e32 v128, s2, v223
	ds_read_b128 v[144:147], v128 offset:49152
	v_add_u32_e32 v129, s2, v226
	ds_read_b128 v[148:151], v129 offset:49152
	v_add_u32_e32 v130, s2, v228
	ds_read_b128 v[152:155], v130 offset:49152
	v_add_u32_e32 v131, s2, v229
	ds_read_b128 v[156:159], v131 offset:49152
	ds_read_b128 v[232:235], v128 offset:53248
	ds_read_b128 v[236:239], v129 offset:53248
	ds_read_b128 v[240:243], v130 offset:53248
	ds_read_b128 v[244:247], v131 offset:53248
	v_lshl_add_u64 v[202:203], v[200:201], 0, s[64:65]
	s_mov_b32 s2, 0x8a40000
	v_add_co_u32_e32 v64, vcc, s2, v202
	s_mov_b32 s2, 0x8a50000
	s_nop 0
	v_addc_co_u32_e32 v65, vcc, 0, v203, vcc
	v_add_co_u32_e32 v66, vcc, s2, v202
	v_lshl_add_u64 v[204:205], v[198:199], 0, s[64:65]
	s_nop 0
	v_addc_co_u32_e32 v67, vcc, 0, v203, vcc
	s_mov_b32 s2, 0x6a40000
	global_load_dwordx4 v[178:181], v[64:65], off
	global_load_dwordx4 v[182:185], v[66:67], off
	v_add_co_u32_e32 v64, vcc, s2, v204
	s_nop 1
	v_addc_co_u32_e32 v65, vcc, 0, v205, vcc
	global_load_dwordx4 v[186:189], v[64:65], off
	v_exp_f32_e32 v190, v120
	v_exp_f32_e32 v191, v121
	v_add_f32_e32 v120, v96, v97
	v_add_f32_e32 v121, v98, v99
	v_exp_f32_e32 v192, v122
	v_add_f32_e32 v120, v120, v121
	v_add_f32_e32 v121, v100, v101
	v_add_f32_e32 v122, v102, v103
	v_exp_f32_e32 v193, v123
	v_add_f32_e32 v121, v121, v122
	v_add_f32_e32 v122, v104, v105
	v_add_f32_e32 v123, v106, v107
	v_add_f32_e32 v122, v122, v123
	v_add_f32_e32 v123, v108, v109
	v_add_f32_e32 v208, v110, v111
	v_add_f32_e32 v123, v123, v208
	v_add_f32_e32 v208, v112, v113
	v_add_f32_e32 v209, v114, v115
	v_add_f32_e32 v208, v208, v209
	s_waitcnt lgkmcnt(7)
	v_mfma_f32_32x32x16_bf16 v[128:143], v[144:147], v[162:165], v[80:95]
	s_waitcnt lgkmcnt(6)
	v_mfma_f32_32x32x16_bf16 v[128:143], v[148:151], v[166:169], v[128:143]
	s_waitcnt lgkmcnt(5)
	v_mfma_f32_32x32x16_bf16 v[128:143], v[152:155], v[170:173], v[128:143]
	s_waitcnt lgkmcnt(4)
	v_mfma_f32_32x32x16_bf16 v[128:143], v[156:159], v[174:177], v[128:143]
	v_exp_f32_e32 v124, v124
	v_exp_f32_e32 v125, v125
	s_waitcnt lgkmcnt(3)
	v_mfma_f32_32x32x16_bf16 v[144:159], v[232:235], v[162:165], v[80:95]
	v_lshl_add_u32 v234, s12, 14, v217
	ds_read_b64_tr_b16 v[64:65], v234 offset:0
	ds_read_b64_tr_b16 v[66:67], v234 offset:0x800
	ds_read_b64_tr_b16 v[68:69], v234 offset:0x1000
	ds_read_b64_tr_b16 v[70:71], v234 offset:0x1800
	ds_read_b64_tr_b16 v[72:73], v234 offset:0x2000
	ds_read_b64_tr_b16 v[74:75], v234 offset:0x2800
	ds_read_b64_tr_b16 v[76:77], v234 offset:0x3000
	ds_read_b64_tr_b16 v[78:79], v234 offset:0x3800
	v_exp_f32_e32 v126, v126
	v_exp_f32_e32 v127, v127
	v_add_f32_e32 v120, v208, v120
	v_add_f32_e32 v208, v116, v117
	v_add_f32_e32 v209, v118, v119
	v_add_f32_e32 v208, v208, v209
	v_add_f32_e32 v121, v208, v121
	s_waitcnt lgkmcnt(10)
	v_mfma_f32_32x32x16_bf16 v[144:159], v[236:239], v[166:169], v[144:159]
	v_add_f32_e32 v208, v190, v191
	v_add_f32_e32 v209, v192, v193
	v_add_f32_e32 v208, v208, v209
	v_add_f32_e32 v122, v122, v208
	v_add_f32_e32 v208, v124, v125
	v_add_f32_e32 v209, v126, v127
	v_add_f32_e32 v208, v208, v209
	s_waitcnt lgkmcnt(9)
	v_mfma_f32_32x32x16_bf16 v[144:159], v[240:243], v[170:173], v[144:159]
	v_add_f32_e32 v123, v123, v208
	v_add_f32_e32 v120, v120, v121
	v_add_f32_e32 v121, v122, v123
	v_add_f32_e32 v231, v120, v121
	v_mov_b32_e32 v232, v231
	v_cvt_pk_bf16_f32 v96, v96, v97
	v_cvt_pk_bf16_f32 v97, v98, v99
	s_waitcnt lgkmcnt(8)
	v_mfma_f32_32x32x16_bf16 v[144:159], v[244:247], v[174:177], v[144:159]
	v_cvt_pk_bf16_f32 v98, v100, v101
	v_cvt_pk_bf16_f32 v99, v102, v103
	v_cvt_pk_bf16_f32 v120, v104, v105
	v_cvt_pk_bf16_f32 v121, v106, v107
	v_cvt_pk_bf16_f32 v122, v108, v109
	v_cvt_pk_bf16_f32 v123, v110, v111
	v_permlane32_swap_b32_e32 v96, v98
	v_permlane32_swap_b32_e32 v97, v99
	v_cvt_pk_bf16_f32 v104, v112, v113
	v_cvt_pk_bf16_f32 v105, v114, v115
	v_cvt_pk_bf16_f32 v106, v116, v117
	v_cvt_pk_bf16_f32 v107, v118, v119
	s_waitcnt lgkmcnt(0)
	v_mfma_f32_32x32x16_bf16 v[0:15], v[96:99], v[64:67], v[0:15]
	v_permlane32_swap_b32_e32 v120, v122
	v_permlane32_swap_b32_e32 v121, v123
	v_cvt_pk_bf16_f32 v100, v190, v191
	v_cvt_pk_bf16_f32 v101, v192, v193
	v_cvt_pk_bf16_f32 v102, v124, v125
	v_cvt_pk_bf16_f32 v103, v126, v127
	v_mfma_f32_32x32x16_bf16 v[0:15], v[120:123], v[68:71], v[0:15]
	v_permlane32_swap_b32_e32 v104, v106
	v_permlane32_swap_b32_e32 v105, v107
	ds_read_b64_tr_b16 v[236:237], v234 offset:0x200
	ds_read_b64_tr_b16 v[238:239], v234 offset:0xa00
	ds_read_b64_tr_b16 v[240:241], v234 offset:0x1200
	ds_read_b64_tr_b16 v[242:243], v234 offset:0x1a00
	ds_read_b64_tr_b16 v[244:245], v234 offset:0x2200
	ds_read_b64_tr_b16 v[246:247], v234 offset:0x2a00
	ds_read_b64_tr_b16 v[190:191], v234 offset:0x3200
	ds_read_b64_tr_b16 v[192:193], v234 offset:0x3a00
	v_mfma_f32_32x32x16_bf16 v[0:15], v[104:107], v[72:75], v[0:15]
	v_permlane32_swap_b32_e32 v100, v102
	v_permlane32_swap_b32_e32 v101, v103
	v_permlane32_swap_b32_e32 v231, v232
	v_max_f32_e32 v108, v128, v129
	v_max3_f32 v109, v130, v131, v145
	v_max3_f32 v108, v108, v144, v146
	v_max3_f32 v108, v108, v147, v132
	v_max3_f32 v109, v109, v134, v135
	v_mfma_f32_32x32x16_bf16 v[0:15], v[100:103], v[76:79], v[0:15]
	v_max3_f32 v208, v108, v133, v148
	v_max3_f32 v209, v109, v150, v151
	ds_read_b64_tr_b16 v[124:125], v234 offset:0x400
	ds_read_b64_tr_b16 v[126:127], v234 offset:0xc00
	ds_read_b64_tr_b16 v[116:117], v234 offset:0x1400
	ds_read_b64_tr_b16 v[118:119], v234 offset:0x1c00
	ds_read_b64_tr_b16 v[112:113], v234 offset:0x2400
	ds_read_b64_tr_b16 v[114:115], v234 offset:0x2c00
	ds_read_b64_tr_b16 v[108:109], v234 offset:0x3400
	ds_read_b64_tr_b16 v[110:111], v234 offset:0x3c00
	s_waitcnt lgkmcnt(8)
	v_mfma_f32_32x32x16_bf16 v[48:63], v[96:99], v[236:239], v[48:63]
	v_max3_f32 v208, v208, v149, v136
	v_max3_f32 v209, v209, v138, v139
	v_max3_f32 v208, v208, v137, v152
	v_max3_f32 v209, v209, v154, v155
	v_max3_f32 v208, v208, v153, v140
	v_max3_f32 v209, v209, v142, v143
	v_max3_f32 v208, v208, v141, v156
	v_mfma_f32_32x32x16_bf16 v[48:63], v[120:123], v[240:243], v[48:63]
	v_max3_f32 v209, v209, v158, v159
	v_max3_f32 v208, v208, v157, v209
	v_mov_b32_e32 v209, v208
	s_nop 1
	v_permlane32_swap_b32_e32 v208, v209
	v_mfma_f32_32x32x16_bf16 v[48:63], v[104:107], v[244:247], v[48:63]
	v_max_f32_e32 v233, v208, v209
	v_mfma_f32_32x32x16_bf16 v[48:63], v[100:103], v[190:193], v[48:63]
	ds_read_b64_tr_b16 v[190:191], v234 offset:0x600
	ds_read_b64_tr_b16 v[192:193], v234 offset:0xe00
	ds_read_b64_tr_b16 v[236:237], v234 offset:0x1600
	ds_read_b64_tr_b16 v[238:239], v234 offset:0x1e00
	ds_read_b64_tr_b16 v[240:241], v234 offset:0x2600
	ds_read_b64_tr_b16 v[242:243], v234 offset:0x2e00
	ds_read_b64_tr_b16 v[244:245], v234 offset:0x3600
	ds_read_b64_tr_b16 v[246:247], v234 offset:0x3e00
	s_mov_b32 s2, 0x4138aa3b
	v_cmp_ge_f32_e32 vcc, s2, v233
	s_cmp_eq_u64 vcc, exec
	s_cbranch_scc0 .LBB0_836
	v_mov_b32_e32 v233, 1.0
.LBB0_825:
	s_waitcnt lgkmcnt(8)
	v_mfma_f32_32x32x16_bf16 v[32:47], v[96:99], v[124:127], v[32:47]
	v_exp_f32_e32 v128, v128
	v_exp_f32_e32 v129, v129
	v_exp_f32_e32 v130, v130
	v_mfma_f32_32x32x16_bf16 v[32:47], v[120:123], v[116:119], v[32:47]
	v_exp_f32_e32 v131, v131
	v_exp_f32_e32 v132, v132
	v_exp_f32_e32 v133, v133
	v_mfma_f32_32x32x16_bf16 v[32:47], v[104:107], v[112:115], v[32:47]
	v_exp_f32_e32 v134, v134
	v_exp_f32_e32 v135, v135
	v_exp_f32_e32 v136, v136
	v_mfma_f32_32x32x16_bf16 v[32:47], v[100:103], v[108:111], v[32:47]
	v_exp_f32_e32 v137, v137
	v_exp_f32_e32 v138, v138
	v_exp_f32_e32 v139, v139
	s_waitcnt lgkmcnt(0)
	s_lshl_b32 s2, s41, 14
	s_add_i32 s2, s2, 0
	v_add_u32_e32 v64, s2, v218
	s_lshl_b32 s3, s41, 13
	s_waitcnt vmcnt(2)
	ds_write_b128 v64, v[178:181]
	v_add_u32_e32 v64, s2, v219
	s_sub_i32 s2, s2, s3
	s_waitcnt vmcnt(1)
	ds_write_b128 v64, v[182:185]
	v_add_u32_e32 v64, s2, v220
	s_waitcnt vmcnt(0)
	ds_write_b128 v64, v[186:189] offset:49152
	v_mfma_f32_32x32x16_bf16 v[16:31], v[96:99], v[190:193], v[16:31]
	v_exp_f32_e32 v140, v140
	v_exp_f32_e32 v141, v141
	v_exp_f32_e32 v142, v142
	v_mfma_f32_32x32x16_bf16 v[16:31], v[120:123], v[236:239], v[16:31]
	v_exp_f32_e32 v143, v143
	v_exp_f32_e32 v144, v144
	v_exp_f32_e32 v145, v145
	v_cmp_gt_f32_e32 vcc, 1.0, v233
	v_mfma_f32_32x32x16_bf16 v[16:31], v[104:107], v[240:243], v[16:31]
	v_exp_f32_e32 v146, v146
	v_exp_f32_e32 v147, v147
	v_exp_f32_e32 v148, v148
	v_mfma_f32_32x32x16_bf16 v[16:31], v[100:103], v[244:247], v[16:31]
	v_exp_f32_e32 v149, v149
	v_exp_f32_e32 v150, v150
	v_exp_f32_e32 v151, v151
	s_cbranch_vccz .LBB0_829
	s_and_saveexec_b64 s[12:13], s[0:1]
	ds_write_b32 v214, v233 offset:128
	s_or_b64 exec, exec, s[12:13]
	s_waitcnt lgkmcnt(0)
	v_add_u32_e32 v108, v213, v160
	ds_read_b128 v[96:99], v108 offset:224
	ds_read_b128 v[100:103], v108 offset:192
	ds_read_b128 v[104:107], v108 offset:160
	ds_read_b128 v[108:111], v108 offset:128
	s_waitcnt lgkmcnt(3)
	v_pk_mul_f32 v[12:13], v[12:13], v[96:97]
	s_waitcnt lgkmcnt(2)
	v_pk_mul_f32 v[8:9], v[8:9], v[100:101]
	s_waitcnt lgkmcnt(1)
	v_pk_mul_f32 v[4:5], v[4:5], v[104:105]
	v_pk_mul_f32 v[14:15], v[14:15], v[98:99]
	v_pk_mul_f32 v[10:11], v[10:11], v[102:103]
	v_pk_mul_f32 v[6:7], v[6:7], v[106:107]
	s_waitcnt lgkmcnt(0)
	v_pk_mul_f32 v[2:3], v[2:3], v[110:111]
	v_pk_mul_f32 v[0:1], v[0:1], v[108:109]
	v_pk_mul_f32 v[60:61], v[60:61], v[96:97]
	v_pk_mul_f32 v[56:57], v[56:57], v[100:101]
	v_pk_mul_f32 v[52:53], v[52:53], v[104:105]
	v_pk_mul_f32 v[62:63], v[62:63], v[98:99]
	v_pk_mul_f32 v[58:59], v[58:59], v[102:103]
	v_pk_mul_f32 v[54:55], v[54:55], v[106:107]
	v_pk_mul_f32 v[50:51], v[50:51], v[110:111]
	v_pk_mul_f32 v[48:49], v[48:49], v[108:109]
	v_pk_mul_f32 v[44:45], v[44:45], v[96:97]
	v_pk_mul_f32 v[40:41], v[40:41], v[100:101]
	v_pk_mul_f32 v[36:37], v[36:37], v[104:105]
	v_pk_mul_f32 v[46:47], v[46:47], v[98:99]
	v_pk_mul_f32 v[42:43], v[42:43], v[102:103]
	v_pk_mul_f32 v[38:39], v[38:39], v[106:107]
	v_pk_mul_f32 v[34:35], v[34:35], v[110:111]
	v_pk_mul_f32 v[32:33], v[32:33], v[108:109]
	v_pk_mul_f32 v[28:29], v[28:29], v[96:97]
	v_pk_mul_f32 v[24:25], v[24:25], v[100:101]
	v_pk_mul_f32 v[20:21], v[20:21], v[104:105]
	v_pk_mul_f32 v[30:31], v[30:31], v[98:99]
	v_pk_mul_f32 v[26:27], v[26:27], v[102:103]
	v_pk_mul_f32 v[22:23], v[22:23], v[106:107]
	v_pk_mul_f32 v[18:19], v[18:19], v[110:111]
	v_pk_mul_f32 v[16:17], v[16:17], v[108:109]
; #define SBAR() __builtin_amdgcn_sched_barrier(0)
; #define SLOAD(k0) do { vs0 = *reinterpret_cast<const bf16x8*>(&Vh[(size_t)((k0) + sr) * DM + sc]); vs1 = *reinterpret_cast<const bf16x8*>(&Vh[(size_t)((k0) + 32 + sr) * DM + sc]); \
;     ks = *reinterpret_cast<const bf16x8*>(&Kh[(size_t)((k0) + kr) * DM + kc]); } while (0)
; #define SWRITE(s) do { *(bf16x8*)(V_lds + (s) * SHM_V + vst0) = vs0; *(bf16x8*)(V_lds + (s) * SHM_V + vst1) = vs1; *(bf16x8*)(K_lds + (s) * SHM_K64 + kst) = ks; } while (0)
; #define RESC(a) do { if (__any((a) < 1.f)) { if (hi == 0) al_l[r32] = (a); asm volatile("s_waitcnt lgkmcnt(0)" ::: "memory"); \
;     _Pragma("unroll") for (int d = 0; d < 4; ++d) _Pragma("unroll") for (int r = 0; r < 16; ++r) o[d][r] *= al_l[crow(r, hi)]; } } while (0)
; #define ROT() do { s_prev = s_cur; s_cur = s_next; s_next = (s_next == DA_NBUF - 1) ? 0 : s_next + 1; } while (0)
; __device__ __forceinline__ void diff_pass(const bf16_t* __restrict__ Qb, const bf16_t* __restrict__ Kh, const bf16_t* __restrict__ Vh, int seq, char* lds, f32x16 (&o)[4], const int wave_) {
;     ...
;         SBAR(); qkt64c(pB0, pB1, K_lds + s_cur * SHM_K64, qr, negm, r32, hi); FIN(pA0, pA1, alA); SBAR();
;         YSEG(pB0, pB1, alB, s_prev);
;         SWRITE(s_next); RESC(alB); __syncthreads(); ROT();
;         SLOAD((j + 2) * 64);
;         SBAR(); qkt64c(pA0, pA1, K_lds + s_cur * SHM_K64, qr, negm, r32, hi); FIN(pB0, pB1, alB); SBAR();
;         YSEG(pA0, pA1, alA, s_prev);
.LBB0_829:
	v_add_co_u32_e32 v96, vcc, 0x8a60000, v202
	s_waitcnt lgkmcnt(0)
	s_nop 0
	v_addc_co_u32_e32 v97, vcc, 0, v203, vcc
	v_add_co_u32_e32 v98, vcc, 0x8a70000, v202
	s_nop 1
	v_addc_co_u32_e32 v99, vcc, 0, v203, vcc
	v_add_co_u32_e32 v100, vcc, 0x6a60000, v204
	s_nop 1
	v_addc_co_u32_e32 v101, vcc, 0, v205, vcc
	s_barrier
	v_add_u32_e32 v102, s2, v223
	ds_read_b128 v[112:115], v102 offset:49152
	v_add_u32_e32 v103, s2, v226
	ds_read_b128 v[116:119], v103 offset:49152
	v_add_u32_e32 v104, s2, v228
	ds_read_b128 v[120:123], v104 offset:49152
	v_add_u32_e32 v105, s2, v229
	ds_read_b128 v[124:127], v105 offset:49152
	ds_read_b128 v[190:193], v102 offset:53248
	ds_read_b128 v[202:205], v103 offset:53248
	ds_read_b128 v[234:237], v104 offset:53248
	ds_read_b128 v[238:241], v105 offset:53248
	global_load_dwordx4 v[178:181], v[96:97], off
	global_load_dwordx4 v[182:185], v[98:99], off
	global_load_dwordx4 v[186:189], v[100:101], off
	v_exp_f32_e32 v208, v152
	v_exp_f32_e32 v209, v153
	v_add_f32_e32 v152, v128, v129
	v_add_f32_e32 v153, v130, v131
	v_exp_f32_e32 v210, v154
	v_add_f32_e32 v152, v152, v153
	v_add_f32_e32 v153, v132, v133
	v_add_f32_e32 v154, v134, v135
	v_exp_f32_e32 v211, v155
	v_add_f32_e32 v153, v153, v154
	v_add_f32_e32 v154, v136, v137
	v_add_f32_e32 v155, v138, v139
	v_add_f32_e32 v154, v154, v155
	v_add_f32_e32 v155, v140, v141
	v_exp_f32_e32 v156, v156
	v_exp_f32_e32 v157, v157
	v_exp_f32_e32 v158, v158
	v_exp_f32_e32 v159, v159
	s_waitcnt lgkmcnt(7)
	v_mfma_f32_32x32x16_bf16 v[96:111], v[112:115], v[162:165], v[80:95]
	s_waitcnt lgkmcnt(6)
	v_mfma_f32_32x32x16_bf16 v[96:111], v[116:119], v[166:169], v[96:111]
	s_waitcnt lgkmcnt(5)
	v_mfma_f32_32x32x16_bf16 v[96:111], v[120:123], v[170:173], v[96:111]
	s_waitcnt lgkmcnt(4)
	v_mfma_f32_32x32x16_bf16 v[96:111], v[124:127], v[174:177], v[96:111]
	s_waitcnt lgkmcnt(3)
	v_mfma_f32_32x32x16_bf16 v[112:127], v[190:193], v[162:165], v[80:95]
	v_add_f32_e32 v190, v142, v143
	v_add_f32_e32 v155, v155, v190
	v_add_f32_e32 v190, v144, v145
	v_add_f32_e32 v191, v146, v147
	v_add_f32_e32 v190, v190, v191
	v_add_f32_e32 v152, v152, v190
	v_add_f32_e32 v190, v148, v149
	s_waitcnt lgkmcnt(2)
	v_mfma_f32_32x32x16_bf16 v[112:127], v[202:205], v[166:169], v[112:127]
	v_lshl_add_u32 v205, s42, 14, v217
	ds_read_b64_tr_b16 v[64:65], v205 offset:0
	ds_read_b64_tr_b16 v[66:67], v205 offset:0x800
	ds_read_b64_tr_b16 v[68:69], v205 offset:0x1000
	ds_read_b64_tr_b16 v[70:71], v205 offset:0x1800
	ds_read_b64_tr_b16 v[72:73], v205 offset:0x2000
	ds_read_b64_tr_b16 v[74:75], v205 offset:0x2800
	ds_read_b64_tr_b16 v[76:77], v205 offset:0x3000
	ds_read_b64_tr_b16 v[78:79], v205 offset:0x3800
	v_add_f32_e32 v191, v150, v151
	v_add_f32_e32 v190, v190, v191
	v_add_f32_e32 v153, v153, v190
	v_add_f32_e32 v190, v208, v209
	v_add_f32_e32 v191, v210, v211
	v_add_f32_e32 v190, v190, v191
	v_add_f32_e32 v154, v154, v190
	s_waitcnt lgkmcnt(9)
	v_mfma_f32_32x32x16_bf16 v[112:127], v[234:237], v[170:173], v[112:127]
	v_add_f32_e32 v190, v156, v157
	v_add_f32_e32 v191, v158, v159
	v_add_f32_e32 v190, v190, v191
	v_add_f32_e32 v155, v155, v190
	v_add_f32_e32 v152, v152, v153
	v_add_f32_e32 v153, v154, v155
	v_add_f32_e32 v203, v152, v153
	s_waitcnt lgkmcnt(8)
	v_mfma_f32_32x32x16_bf16 v[112:127], v[238:241], v[174:177], v[112:127]
	v_mov_b32_e32 v204, v203
	v_cvt_pk_bf16_f32 v152, v128, v129
	v_cvt_pk_bf16_f32 v153, v130, v131
	v_cvt_pk_bf16_f32 v154, v132, v133
	v_cvt_pk_bf16_f32 v155, v134, v135
	v_cvt_pk_bf16_f32 v136, v136, v137
	v_cvt_pk_bf16_f32 v137, v138, v139
	v_cvt_pk_bf16_f32 v138, v140, v141
	v_cvt_pk_bf16_f32 v139, v142, v143
	v_permlane32_swap_b32_e32 v152, v154
	v_permlane32_swap_b32_e32 v153, v155
	v_cvt_pk_bf16_f32 v132, v144, v145
	v_cvt_pk_bf16_f32 v133, v146, v147
	v_cvt_pk_bf16_f32 v134, v148, v149
	v_cvt_pk_bf16_f32 v135, v150, v151
	s_waitcnt lgkmcnt(0)
	v_mfma_f32_32x32x16_bf16 v[0:15], v[152:155], v[64:67], v[0:15]
	v_permlane32_swap_b32_e32 v136, v138
	v_permlane32_swap_b32_e32 v137, v139
	v_cvt_pk_bf16_f32 v128, v208, v209
	v_cvt_pk_bf16_f32 v129, v210, v211
	v_cvt_pk_bf16_f32 v130, v156, v157
	v_cvt_pk_bf16_f32 v131, v158, v159
	v_mfma_f32_32x32x16_bf16 v[0:15], v[136:139], v[68:71], v[0:15]
	v_permlane32_swap_b32_e32 v132, v134
	v_permlane32_swap_b32_e32 v133, v135
	ds_read_b64_tr_b16 v[190:191], v205 offset:0x200
	ds_read_b64_tr_b16 v[192:193], v205 offset:0xa00
	ds_read_b64_tr_b16 v[234:235], v205 offset:0x1200
	ds_read_b64_tr_b16 v[236:237], v205 offset:0x1a00
	ds_read_b64_tr_b16 v[238:239], v205 offset:0x2200
	ds_read_b64_tr_b16 v[240:241], v205 offset:0x2a00
	ds_read_b64_tr_b16 v[242:243], v205 offset:0x3200
	ds_read_b64_tr_b16 v[244:245], v205 offset:0x3a00
	v_mfma_f32_32x32x16_bf16 v[0:15], v[132:135], v[72:75], v[0:15]
	v_permlane32_swap_b32_e32 v128, v130
	v_permlane32_swap_b32_e32 v129, v131
	v_permlane32_swap_b32_e32 v203, v204
	v_max_f32_e32 v140, v96, v97
	v_max3_f32 v140, v140, v112, v114
	v_max3_f32 v141, v98, v99, v113
	v_max3_f32 v140, v140, v115, v100
	v_max3_f32 v141, v141, v102, v103
	v_mfma_f32_32x32x16_bf16 v[0:15], v[128:131], v[76:79], v[0:15]
	v_max3_f32 v202, v140, v101, v116
	v_max3_f32 v208, v141, v118, v119
	ds_read_b64_tr_b16 v[156:157], v205 offset:0x400
	ds_read_b64_tr_b16 v[158:159], v205 offset:0xc00
	ds_read_b64_tr_b16 v[148:149], v205 offset:0x1400
	ds_read_b64_tr_b16 v[150:151], v205 offset:0x1c00
	ds_read_b64_tr_b16 v[144:145], v205 offset:0x2400
	ds_read_b64_tr_b16 v[146:147], v205 offset:0x2c00
	ds_read_b64_tr_b16 v[140:141], v205 offset:0x3400
	ds_read_b64_tr_b16 v[142:143], v205 offset:0x3c00
	s_waitcnt lgkmcnt(8)
	v_mfma_f32_32x32x16_bf16 v[48:63], v[152:155], v[190:193], v[48:63]
	v_max3_f32 v190, v202, v117, v104
	v_max3_f32 v191, v208, v106, v107
	v_max3_f32 v190, v190, v105, v120
	v_max3_f32 v191, v191, v122, v123
	v_max3_f32 v190, v190, v121, v108
	v_max3_f32 v191, v191, v110, v111
	v_max3_f32 v190, v190, v109, v124
	v_mfma_f32_32x32x16_bf16 v[48:63], v[136:139], v[234:237], v[48:63]
	v_max3_f32 v191, v191, v126, v127
	v_max3_f32 v190, v190, v125, v191
	v_mov_b32_e32 v191, v190
	s_nop 1
	v_permlane32_swap_b32_e32 v190, v191
	v_mfma_f32_32x32x16_bf16 v[48:63], v[132:135], v[238:241], v[48:63]
	v_max_f32_e32 v234, v190, v191
	v_mfma_f32_32x32x16_bf16 v[48:63], v[128:131], v[242:245], v[48:63]
	s_mov_b32 s2, 0x4138aa3b
	v_cmp_ge_f32_e32 vcc, s2, v234
	s_cmp_eq_u64 vcc, exec
	v_mov_b32_e32 v202, 1.0
	s_cbranch_scc0 .LBB0_837

.LBB0_846:
	s_lshl_b32 s2, s30, 13
	s_add_i32 s2, s2, 0
	v_add_u32_e32 v128, s2, v227
	ds_read_b128 v[144:147], v128 offset:49152
	v_add_u32_e32 v129, s2, v231
	ds_read_b128 v[148:151], v129 offset:49152
	v_add_u32_e32 v130, s2, v232
	ds_read_b128 v[152:155], v130 offset:49152
	v_add_u32_e32 v131, s2, v233
	ds_read_b128 v[156:159], v131 offset:49152
	ds_read_b128 v[190:193], v128 offset:53248
	ds_read_b128 v[236:239], v129 offset:53248
	ds_read_b128 v[240:243], v130 offset:53248
	ds_read_b128 v[244:247], v131 offset:53248
	v_lshl_add_u64 v[202:203], v[200:201], 0, s[64:65]
	s_mov_b32 s2, 0x8a40000
	v_add_co_u32_e32 v64, vcc, s2, v202
	s_mov_b32 s2, 0x8a50000
	s_nop 0
	v_addc_co_u32_e32 v65, vcc, 0, v203, vcc
	v_add_co_u32_e32 v66, vcc, s2, v202
	v_lshl_add_u64 v[204:205], v[198:199], 0, s[64:65]
	s_nop 0
	v_addc_co_u32_e32 v67, vcc, 0, v203, vcc
	s_mov_b32 s2, 0x6a40000
	global_load_dwordx4 v[178:181], v[64:65], off
	global_load_dwordx4 v[182:185], v[66:67], off
	v_add_co_u32_e32 v64, vcc, s2, v204
	s_nop 1
	v_addc_co_u32_e32 v65, vcc, 0, v205, vcc
	global_load_dwordx4 v[186:189], v[64:65], off offset:128
	v_exp_f32_e32 v208, v120
	v_exp_f32_e32 v209, v121
	v_add_f32_e32 v120, v96, v97
	v_add_f32_e32 v121, v98, v99
	v_exp_f32_e32 v210, v122
	v_add_f32_e32 v120, v120, v121
	v_add_f32_e32 v121, v100, v101
	v_add_f32_e32 v122, v102, v103
	v_exp_f32_e32 v211, v123
	v_add_f32_e32 v121, v121, v122
	v_add_f32_e32 v122, v104, v105
	v_add_f32_e32 v123, v106, v107
	v_add_f32_e32 v122, v122, v123
	v_add_f32_e32 v123, v108, v109
	v_exp_f32_e32 v124, v124
	v_exp_f32_e32 v125, v125
	v_exp_f32_e32 v126, v126
	v_exp_f32_e32 v127, v127
	v_cvt_pk_bf16_f32 v96, v96, v97
	s_waitcnt lgkmcnt(7)
	v_mfma_f32_32x32x16_bf16 v[128:143], v[144:147], v[162:165], v[80:95]
	s_waitcnt lgkmcnt(6)
	v_mfma_f32_32x32x16_bf16 v[128:143], v[148:151], v[166:169], v[128:143]
	s_waitcnt lgkmcnt(5)
	v_mfma_f32_32x32x16_bf16 v[128:143], v[152:155], v[170:173], v[128:143]
	s_waitcnt lgkmcnt(4)
	v_mfma_f32_32x32x16_bf16 v[128:143], v[156:159], v[174:177], v[128:143]
	v_cvt_pk_bf16_f32 v97, v98, v99
	v_cvt_pk_bf16_f32 v98, v100, v101
	v_cvt_pk_bf16_f32 v99, v102, v103
	s_nop 0
	v_permlane32_swap_b32_e32 v96, v98
	s_waitcnt lgkmcnt(3)
	v_mfma_f32_32x32x16_bf16 v[144:159], v[190:193], v[162:165], v[80:95]
	v_add_f32_e32 v190, v110, v111
	v_add_f32_e32 v123, v123, v190
	v_add_f32_e32 v190, v112, v113
	v_add_f32_e32 v191, v114, v115
	v_add_f32_e32 v190, v190, v191
	v_add_f32_e32 v120, v190, v120
	v_add_f32_e32 v190, v116, v117
	s_waitcnt lgkmcnt(2)
	v_mfma_f32_32x32x16_bf16 v[144:159], v[236:239], v[166:169], v[144:159]
	v_lshl_add_u32 v238, s12, 14, v221
	ds_read_b64_tr_b16 v[64:65], v238 offset:0
	ds_read_b64_tr_b16 v[66:67], v238 offset:0x800
	ds_read_b64_tr_b16 v[68:69], v238 offset:0x1000
	ds_read_b64_tr_b16 v[70:71], v238 offset:0x1800
	ds_read_b64_tr_b16 v[72:73], v238 offset:0x2000
	ds_read_b64_tr_b16 v[74:75], v238 offset:0x2800
	ds_read_b64_tr_b16 v[76:77], v238 offset:0x3000
	ds_read_b64_tr_b16 v[78:79], v238 offset:0x3800
	v_add_f32_e32 v191, v118, v119
	v_add_f32_e32 v190, v190, v191
	v_add_f32_e32 v121, v190, v121
	v_add_f32_e32 v190, v208, v209
	v_add_f32_e32 v191, v210, v211
	v_add_f32_e32 v190, v190, v191
	v_add_f32_e32 v122, v122, v190
	s_waitcnt lgkmcnt(9)
	v_mfma_f32_32x32x16_bf16 v[144:159], v[240:243], v[170:173], v[144:159]
	v_add_f32_e32 v190, v124, v125
	v_add_f32_e32 v191, v126, v127
	v_add_f32_e32 v190, v190, v191
	v_add_f32_e32 v123, v123, v190
	v_add_f32_e32 v120, v120, v121
	v_add_f32_e32 v121, v122, v123
	v_add_f32_e32 v235, v120, v121
	s_waitcnt lgkmcnt(8)
	v_mfma_f32_32x32x16_bf16 v[144:159], v[244:247], v[174:177], v[144:159]
	v_mov_b32_e32 v236, v235
	v_cvt_pk_bf16_f32 v120, v104, v105
	v_cvt_pk_bf16_f32 v121, v106, v107
	v_cvt_pk_bf16_f32 v122, v108, v109
	v_cvt_pk_bf16_f32 v123, v110, v111
	v_permlane32_swap_b32_e32 v97, v99
	v_cvt_pk_bf16_f32 v104, v112, v113
	v_cvt_pk_bf16_f32 v105, v114, v115
	v_cvt_pk_bf16_f32 v106, v116, v117
	v_cvt_pk_bf16_f32 v107, v118, v119
	s_waitcnt lgkmcnt(0)
	v_mfma_f32_32x32x16_bf16 v[0:15], v[96:99], v[64:67], v[0:15]
	v_permlane32_swap_b32_e32 v120, v122
	v_permlane32_swap_b32_e32 v121, v123
	v_cvt_pk_bf16_f32 v100, v208, v209
	v_cvt_pk_bf16_f32 v101, v210, v211
	v_cvt_pk_bf16_f32 v102, v124, v125
	v_cvt_pk_bf16_f32 v103, v126, v127
	v_mfma_f32_32x32x16_bf16 v[0:15], v[120:123], v[68:71], v[0:15]
	v_permlane32_swap_b32_e32 v104, v106
	v_permlane32_swap_b32_e32 v105, v107
	ds_read_b64_tr_b16 v[190:191], v238 offset:0x200
	ds_read_b64_tr_b16 v[192:193], v238 offset:0xa00
	ds_read_b64_tr_b16 v[240:241], v238 offset:0x1200
	ds_read_b64_tr_b16 v[242:243], v238 offset:0x1a00
	ds_read_b64_tr_b16 v[244:245], v238 offset:0x2200
	ds_read_b64_tr_b16 v[246:247], v238 offset:0x2a00
	ds_read_b64_tr_b16 v[208:209], v238 offset:0x3200
	ds_read_b64_tr_b16 v[210:211], v238 offset:0x3a00
	v_mfma_f32_32x32x16_bf16 v[0:15], v[104:107], v[72:75], v[0:15]
	v_permlane32_swap_b32_e32 v100, v102
	v_permlane32_swap_b32_e32 v101, v103
	v_permlane32_swap_b32_e32 v235, v236
	v_max_f32_e32 v108, v128, v129
	v_max3_f32 v108, v108, v144, v146
	v_max3_f32 v109, v130, v131, v145
	v_max3_f32 v108, v108, v147, v132
	v_max3_f32 v109, v109, v134, v135
	v_mfma_f32_32x32x16_bf16 v[0:15], v[100:103], v[76:79], v[0:15]
	v_max3_f32 v237, v108, v133, v148
	v_max3_f32 v239, v109, v150, v151
	ds_read_b64_tr_b16 v[124:125], v238 offset:0x400
	ds_read_b64_tr_b16 v[126:127], v238 offset:0xc00
	ds_read_b64_tr_b16 v[116:117], v238 offset:0x1400
	ds_read_b64_tr_b16 v[118:119], v238 offset:0x1c00
	ds_read_b64_tr_b16 v[112:113], v238 offset:0x2400
	ds_read_b64_tr_b16 v[114:115], v238 offset:0x2c00
	ds_read_b64_tr_b16 v[108:109], v238 offset:0x3400
	ds_read_b64_tr_b16 v[110:111], v238 offset:0x3c00
	s_waitcnt lgkmcnt(8)
	v_mfma_f32_32x32x16_bf16 v[48:63], v[96:99], v[190:193], v[48:63]
	v_max3_f32 v190, v237, v149, v136
	v_max3_f32 v191, v239, v138, v139
	v_max3_f32 v190, v190, v137, v152
	v_max3_f32 v191, v191, v154, v155
	v_max3_f32 v190, v190, v153, v140
	v_max3_f32 v191, v191, v142, v143
	v_max3_f32 v190, v190, v141, v156
	v_mfma_f32_32x32x16_bf16 v[48:63], v[120:123], v[240:243], v[48:63]
	v_max3_f32 v191, v191, v158, v159
	v_max3_f32 v190, v190, v157, v191
	v_mov_b32_e32 v191, v190
	s_nop 1
	v_permlane32_swap_b32_e32 v190, v191
	v_mfma_f32_32x32x16_bf16 v[48:63], v[104:107], v[244:247], v[48:63]
	v_max_f32_e32 v237, v190, v191
	v_mfma_f32_32x32x16_bf16 v[48:63], v[100:103], v[208:211], v[48:63]
	ds_read_b64_tr_b16 v[190:191], v238 offset:0x600
	ds_read_b64_tr_b16 v[192:193], v238 offset:0xe00
	ds_read_b64_tr_b16 v[208:209], v238 offset:0x1600
	ds_read_b64_tr_b16 v[210:211], v238 offset:0x1e00
	ds_read_b64_tr_b16 v[240:241], v238 offset:0x2600
	ds_read_b64_tr_b16 v[242:243], v238 offset:0x2e00
	ds_read_b64_tr_b16 v[244:245], v238 offset:0x3600
	ds_read_b64_tr_b16 v[246:247], v238 offset:0x3e00
	s_mov_b32 s2, 0x4138aa3b
	v_cmp_ge_f32_e32 vcc, s2, v237
	s_cmp_eq_u64 vcc, exec
	s_cbranch_scc0 .LBB0_859
	v_mov_b32_e32 v237, 1.0
.LBB0_848:
	s_waitcnt lgkmcnt(8)
	v_mfma_f32_32x32x16_bf16 v[32:47], v[96:99], v[124:127], v[32:47]
	v_exp_f32_e32 v128, v128
	v_exp_f32_e32 v129, v129
	v_exp_f32_e32 v130, v130
	v_mfma_f32_32x32x16_bf16 v[32:47], v[120:123], v[116:119], v[32:47]
	v_exp_f32_e32 v131, v131
	v_exp_f32_e32 v132, v132
	v_exp_f32_e32 v133, v133
	v_mfma_f32_32x32x16_bf16 v[32:47], v[104:107], v[112:115], v[32:47]
	v_exp_f32_e32 v134, v134
	v_exp_f32_e32 v135, v135
	v_exp_f32_e32 v136, v136
	v_mfma_f32_32x32x16_bf16 v[32:47], v[100:103], v[108:111], v[32:47]
	v_exp_f32_e32 v137, v137
	v_exp_f32_e32 v138, v138
	v_exp_f32_e32 v139, v139
	s_waitcnt lgkmcnt(0)
	s_lshl_b32 s2, s29, 14
	s_add_i32 s2, s2, 0
	v_add_u32_e32 v64, s2, v222
	s_lshl_b32 s3, s29, 13
	s_waitcnt vmcnt(2)
	ds_write_b128 v64, v[178:181]
	v_add_u32_e32 v64, s2, v223
	s_sub_i32 s2, s2, s3
	s_waitcnt vmcnt(1)
	ds_write_b128 v64, v[182:185]
	v_add_u32_e32 v64, s2, v224
	s_waitcnt vmcnt(0)
	ds_write_b128 v64, v[186:189] offset:49152
	v_mfma_f32_32x32x16_bf16 v[16:31], v[96:99], v[190:193], v[16:31]
	v_exp_f32_e32 v140, v140
	v_exp_f32_e32 v141, v141
	v_exp_f32_e32 v142, v142
	v_mfma_f32_32x32x16_bf16 v[16:31], v[120:123], v[208:211], v[16:31]
	v_exp_f32_e32 v143, v143
	v_exp_f32_e32 v144, v144
	v_exp_f32_e32 v145, v145
	v_cmp_gt_f32_e32 vcc, 1.0, v237
	v_mfma_f32_32x32x16_bf16 v[16:31], v[104:107], v[240:243], v[16:31]
	v_exp_f32_e32 v146, v146
	v_exp_f32_e32 v147, v147
	v_exp_f32_e32 v148, v148
	v_mfma_f32_32x32x16_bf16 v[16:31], v[100:103], v[244:247], v[16:31]
	v_exp_f32_e32 v149, v149
	v_exp_f32_e32 v150, v150
	v_exp_f32_e32 v151, v151
	s_cbranch_vccz .LBB0_852
	s_and_saveexec_b64 s[10:11], s[0:1]
	ds_write_b32 v218, v237 offset:128
	s_or_b64 exec, exec, s[10:11]
	s_waitcnt lgkmcnt(0)
	v_add_u32_e32 v108, v217, v160
	ds_read_b128 v[96:99], v108 offset:224
	ds_read_b128 v[100:103], v108 offset:192
	ds_read_b128 v[104:107], v108 offset:160
	ds_read_b128 v[108:111], v108 offset:128
	s_waitcnt lgkmcnt(3)
	v_pk_mul_f32 v[12:13], v[12:13], v[96:97]
	s_waitcnt lgkmcnt(2)
	v_pk_mul_f32 v[8:9], v[8:9], v[100:101]
	s_waitcnt lgkmcnt(1)
	v_pk_mul_f32 v[4:5], v[4:5], v[104:105]
	v_pk_mul_f32 v[14:15], v[14:15], v[98:99]
	v_pk_mul_f32 v[10:11], v[10:11], v[102:103]
	v_pk_mul_f32 v[6:7], v[6:7], v[106:107]
	s_waitcnt lgkmcnt(0)
	v_pk_mul_f32 v[2:3], v[2:3], v[110:111]
	v_pk_mul_f32 v[0:1], v[0:1], v[108:109]
	v_pk_mul_f32 v[60:61], v[60:61], v[96:97]
	v_pk_mul_f32 v[56:57], v[56:57], v[100:101]
	v_pk_mul_f32 v[52:53], v[52:53], v[104:105]
	v_pk_mul_f32 v[62:63], v[62:63], v[98:99]
	v_pk_mul_f32 v[58:59], v[58:59], v[102:103]
	v_pk_mul_f32 v[54:55], v[54:55], v[106:107]
	v_pk_mul_f32 v[50:51], v[50:51], v[110:111]
	v_pk_mul_f32 v[48:49], v[48:49], v[108:109]
	v_pk_mul_f32 v[44:45], v[44:45], v[96:97]
	v_pk_mul_f32 v[40:41], v[40:41], v[100:101]
	v_pk_mul_f32 v[36:37], v[36:37], v[104:105]
	v_pk_mul_f32 v[46:47], v[46:47], v[98:99]
	v_pk_mul_f32 v[42:43], v[42:43], v[102:103]
	v_pk_mul_f32 v[38:39], v[38:39], v[106:107]
	v_pk_mul_f32 v[34:35], v[34:35], v[110:111]
	v_pk_mul_f32 v[32:33], v[32:33], v[108:109]
	v_pk_mul_f32 v[28:29], v[28:29], v[96:97]
	v_pk_mul_f32 v[24:25], v[24:25], v[100:101]
	v_pk_mul_f32 v[20:21], v[20:21], v[104:105]
	v_pk_mul_f32 v[30:31], v[30:31], v[98:99]
	v_pk_mul_f32 v[26:27], v[26:27], v[102:103]
	v_pk_mul_f32 v[22:23], v[22:23], v[106:107]
	v_pk_mul_f32 v[18:19], v[18:19], v[110:111]
	v_pk_mul_f32 v[16:17], v[16:17], v[108:109]
; #define SBAR() __builtin_amdgcn_sched_barrier(0)
; #define SLOAD(k0) do { vs0 = *reinterpret_cast<const bf16x8*>(&Vh[(size_t)((k0) + sr) * DM + sc]); vs1 = *reinterpret_cast<const bf16x8*>(&Vh[(size_t)((k0) + 32 + sr) * DM + sc]); \
;     ks = *reinterpret_cast<const bf16x8*>(&Kh[(size_t)((k0) + kr) * DM + kc]); } while (0)
; #define SWRITE(s) do { *(bf16x8*)(V_lds + (s) * SHM_V + vst0) = vs0; *(bf16x8*)(V_lds + (s) * SHM_V + vst1) = vs1; *(bf16x8*)(K_lds + (s) * SHM_K64 + kst) = ks; } while (0)
; #define RESC(a) do { if (__any((a) < 1.f)) { if (hi == 0) al_l[r32] = (a); asm volatile("s_waitcnt lgkmcnt(0)" ::: "memory"); \
;     _Pragma("unroll") for (int d = 0; d < 4; ++d) _Pragma("unroll") for (int r = 0; r < 16; ++r) o[d][r] *= al_l[crow(r, hi)]; } } while (0)
; #define ROT() do { s_prev = s_cur; s_cur = s_next; s_next = (s_next == DA_NBUF - 1) ? 0 : s_next + 1; } while (0)
; __device__ __forceinline__ void diff_pass(const bf16_t* __restrict__ Qb, const bf16_t* __restrict__ Kh, const bf16_t* __restrict__ Vh, int seq, char* lds, f32x16 (&o)[4], const int wave_) {
;     ...
;         SBAR(); qkt64c(pB0, pB1, K_lds + s_cur * SHM_K64, qr, negm, r32, hi); FIN(pA0, pA1, alA); SBAR();
;         YSEG(pB0, pB1, alB, s_prev);
;         SWRITE(s_next); RESC(alB); __syncthreads(); ROT();
;         SLOAD((j + 2) * 64);
;         SBAR(); qkt64c(pA0, pA1, K_lds + s_cur * SHM_K64, qr, negm, r32, hi); FIN(pB0, pB1, alB); SBAR();
;         YSEG(pA0, pA1, alA, s_prev);
.LBB0_852:
	v_add_co_u32_e32 v96, vcc, 0x8a60000, v202
	s_waitcnt lgkmcnt(0)
	s_nop 0
	v_addc_co_u32_e32 v97, vcc, 0, v203, vcc
	v_add_co_u32_e32 v98, vcc, 0x8a70000, v202
	s_nop 1
	v_addc_co_u32_e32 v99, vcc, 0, v203, vcc
	v_add_co_u32_e32 v100, vcc, 0x6a60000, v204
	s_nop 1
	v_addc_co_u32_e32 v101, vcc, 0, v205, vcc
	s_barrier
	v_add_u32_e32 v102, s2, v227
	ds_read_b128 v[112:115], v102 offset:49152
	v_add_u32_e32 v103, s2, v231
	ds_read_b128 v[116:119], v103 offset:49152
	v_add_u32_e32 v104, s2, v232
	ds_read_b128 v[120:123], v104 offset:49152
	v_add_u32_e32 v105, s2, v233
	ds_read_b128 v[124:127], v105 offset:49152
	ds_read_b128 v[190:193], v102 offset:53248
	ds_read_b128 v[202:205], v103 offset:53248
	ds_read_b128 v[208:211], v104 offset:53248
	ds_read_b128 v[238:241], v105 offset:53248
	global_load_dwordx4 v[178:181], v[96:97], off
	global_load_dwordx4 v[182:185], v[98:99], off
	global_load_dwordx4 v[186:189], v[100:101], off offset:128
	v_exp_f32_e32 v242, v152
	v_exp_f32_e32 v243, v153
	v_add_f32_e32 v152, v128, v129
	v_add_f32_e32 v153, v130, v131
	v_exp_f32_e32 v244, v154
	v_add_f32_e32 v152, v152, v153
	v_add_f32_e32 v153, v132, v133
	v_add_f32_e32 v154, v134, v135
	v_exp_f32_e32 v245, v155
	v_add_f32_e32 v153, v153, v154
	v_add_f32_e32 v154, v136, v137
	v_add_f32_e32 v155, v138, v139
	v_add_f32_e32 v154, v154, v155
	v_add_f32_e32 v155, v140, v141
	v_exp_f32_e32 v156, v156
	v_exp_f32_e32 v157, v157
	v_exp_f32_e32 v158, v158
	v_exp_f32_e32 v159, v159
	s_waitcnt lgkmcnt(7)
	v_mfma_f32_32x32x16_bf16 v[96:111], v[112:115], v[162:165], v[80:95]
	s_waitcnt lgkmcnt(6)
	v_mfma_f32_32x32x16_bf16 v[96:111], v[116:119], v[166:169], v[96:111]
	s_waitcnt lgkmcnt(5)
	v_mfma_f32_32x32x16_bf16 v[96:111], v[120:123], v[170:173], v[96:111]
	s_waitcnt lgkmcnt(4)
	v_mfma_f32_32x32x16_bf16 v[96:111], v[124:127], v[174:177], v[96:111]
	s_waitcnt lgkmcnt(3)
	v_mfma_f32_32x32x16_bf16 v[112:127], v[190:193], v[162:165], v[80:95]
	v_add_f32_e32 v190, v142, v143
	v_add_f32_e32 v155, v155, v190
	v_add_f32_e32 v190, v144, v145
	v_add_f32_e32 v191, v146, v147
	v_add_f32_e32 v190, v190, v191
	v_add_f32_e32 v152, v152, v190
	v_add_f32_e32 v190, v148, v149
	s_waitcnt lgkmcnt(2)
	v_mfma_f32_32x32x16_bf16 v[112:127], v[202:205], v[166:169], v[112:127]
	v_lshl_add_u32 v205, s30, 14, v221
	ds_read_b64_tr_b16 v[64:65], v205 offset:0
	ds_read_b64_tr_b16 v[66:67], v205 offset:0x800
	ds_read_b64_tr_b16 v[68:69], v205 offset:0x1000
	ds_read_b64_tr_b16 v[70:71], v205 offset:0x1800
	ds_read_b64_tr_b16 v[72:73], v205 offset:0x2000
	ds_read_b64_tr_b16 v[74:75], v205 offset:0x2800
	ds_read_b64_tr_b16 v[76:77], v205 offset:0x3000
	ds_read_b64_tr_b16 v[78:79], v205 offset:0x3800
	v_add_f32_e32 v191, v150, v151
	v_add_f32_e32 v190, v190, v191
	v_add_f32_e32 v153, v153, v190
	v_add_f32_e32 v190, v242, v243
	v_add_f32_e32 v191, v244, v245
	v_add_f32_e32 v190, v190, v191
	v_add_f32_e32 v154, v154, v190
	s_waitcnt lgkmcnt(9)
	v_mfma_f32_32x32x16_bf16 v[112:127], v[208:211], v[170:173], v[112:127]
	v_add_f32_e32 v190, v156, v157
	v_add_f32_e32 v191, v158, v159
	v_add_f32_e32 v190, v190, v191
	v_add_f32_e32 v155, v155, v190
	v_add_f32_e32 v152, v152, v153
	v_add_f32_e32 v153, v154, v155
	v_add_f32_e32 v203, v152, v153
	s_waitcnt lgkmcnt(8)
	v_mfma_f32_32x32x16_bf16 v[112:127], v[238:241], v[174:177], v[112:127]
	v_mov_b32_e32 v204, v203
	v_cvt_pk_bf16_f32 v152, v128, v129
	v_cvt_pk_bf16_f32 v153, v130, v131
	v_cvt_pk_bf16_f32 v154, v132, v133
	v_cvt_pk_bf16_f32 v155, v134, v135
	v_cvt_pk_bf16_f32 v136, v136, v137
	v_cvt_pk_bf16_f32 v137, v138, v139
	v_cvt_pk_bf16_f32 v138, v140, v141
	v_cvt_pk_bf16_f32 v139, v142, v143
	v_permlane32_swap_b32_e32 v152, v154
	v_permlane32_swap_b32_e32 v153, v155
	v_cvt_pk_bf16_f32 v132, v144, v145
	v_cvt_pk_bf16_f32 v133, v146, v147
	v_cvt_pk_bf16_f32 v134, v148, v149
	v_cvt_pk_bf16_f32 v135, v150, v151
	s_waitcnt lgkmcnt(0)
	v_mfma_f32_32x32x16_bf16 v[0:15], v[152:155], v[64:67], v[0:15]
	v_permlane32_swap_b32_e32 v136, v138
	v_permlane32_swap_b32_e32 v137, v139
	v_cvt_pk_bf16_f32 v128, v242, v243
	v_cvt_pk_bf16_f32 v129, v244, v245
	v_cvt_pk_bf16_f32 v130, v156, v157
	v_cvt_pk_bf16_f32 v131, v158, v159
	v_mfma_f32_32x32x16_bf16 v[0:15], v[136:139], v[68:71], v[0:15]
	v_permlane32_swap_b32_e32 v132, v134
	v_permlane32_swap_b32_e32 v133, v135
	ds_read_b64_tr_b16 v[190:191], v205 offset:0x200
	ds_read_b64_tr_b16 v[192:193], v205 offset:0xa00
	ds_read_b64_tr_b16 v[208:209], v205 offset:0x1200
	ds_read_b64_tr_b16 v[210:211], v205 offset:0x1a00
	ds_read_b64_tr_b16 v[238:239], v205 offset:0x2200
	ds_read_b64_tr_b16 v[240:241], v205 offset:0x2a00
	ds_read_b64_tr_b16 v[242:243], v205 offset:0x3200
	ds_read_b64_tr_b16 v[244:245], v205 offset:0x3a00
	v_mfma_f32_32x32x16_bf16 v[0:15], v[132:135], v[72:75], v[0:15]
	v_permlane32_swap_b32_e32 v128, v130
	v_permlane32_swap_b32_e32 v129, v131
	v_permlane32_swap_b32_e32 v203, v204
	v_max_f32_e32 v140, v96, v97
	v_max3_f32 v140, v140, v112, v114
	v_max3_f32 v141, v98, v99, v113
	v_max3_f32 v140, v140, v115, v100
	v_max3_f32 v141, v141, v102, v103
	v_mfma_f32_32x32x16_bf16 v[0:15], v[128:131], v[76:79], v[0:15]
	v_max3_f32 v202, v140, v101, v116
	v_max3_f32 v246, v141, v118, v119
	ds_read_b64_tr_b16 v[156:157], v205 offset:0x400
	ds_read_b64_tr_b16 v[158:159], v205 offset:0xc00
	ds_read_b64_tr_b16 v[148:149], v205 offset:0x1400
	ds_read_b64_tr_b16 v[150:151], v205 offset:0x1c00
	ds_read_b64_tr_b16 v[144:145], v205 offset:0x2400
	ds_read_b64_tr_b16 v[146:147], v205 offset:0x2c00
	ds_read_b64_tr_b16 v[140:141], v205 offset:0x3400
	ds_read_b64_tr_b16 v[142:143], v205 offset:0x3c00
	s_waitcnt lgkmcnt(8)
	v_mfma_f32_32x32x16_bf16 v[48:63], v[152:155], v[190:193], v[48:63]
	v_max3_f32 v190, v202, v117, v104
	v_max3_f32 v191, v246, v106, v107
	v_max3_f32 v190, v190, v105, v120
	v_max3_f32 v191, v191, v122, v123
	v_max3_f32 v190, v190, v121, v108
	v_max3_f32 v191, v191, v110, v111
	v_max3_f32 v190, v190, v109, v124
	v_mfma_f32_32x32x16_bf16 v[48:63], v[136:139], v[208:211], v[48:63]
	v_max3_f32 v191, v191, v126, v127
	v_max3_f32 v190, v190, v125, v191
	v_mov_b32_e32 v191, v190
	s_nop 1
	v_permlane32_swap_b32_e32 v190, v191
	v_mfma_f32_32x32x16_bf16 v[48:63], v[132:135], v[238:241], v[48:63]
	v_max_f32_e32 v238, v190, v191
	v_mfma_f32_32x32x16_bf16 v[48:63], v[128:131], v[242:245], v[48:63]
	s_mov_b32 s2, 0x4138aa3b
	v_cmp_ge_f32_e32 vcc, s2, v238
	s_cmp_eq_u64 vcc, exec
	v_mov_b32_e32 v202, 1.0
	s_cbranch_scc0 .LBB0_860
